# GEMM phases P2/P6/P10: accumulator zeroing removed, first K half-step peeled with MFMA C=0 (on top of bias-in-accumulator P9 epilogue)
# speedup vs baseline: 1.0127x; 1.0039x over previous
.LBB0_325:
	s_ashr_i32 s15, s12, 31
	s_mov_b32 s14, s12
	s_lshl_b64 s[14:15], s[14:15], 20
	s_add_u32 s14, s28, s14
	s_addc_u32 s15, s29, s15
	s_and_b64 s[16:17], s[2:3], exec
	s_cselect_b32 s74, s15, s21
	s_cselect_b32 s75, s14, s20
	s_ashr_i32 s17, s13, 31
	s_mov_b32 s16, s13
	s_lshl_b64 s[16:17], s[16:17], 20
	s_add_u32 s16, s30, s16
	s_addc_u32 s17, s31, s17
	s_and_b64 s[2:3], s[2:3], exec
	s_cselect_b32 s2, s17, s23
	s_cselect_b32 s3, s16, s22
	s_add_u32 s76, s22, 0x100
	v_lshl_add_u64 v[144:145], s[20:21], 0, v[140:141]
	v_lshl_add_u64 v[146:147], s[20:21], 0, v[142:143]
	s_addc_u32 s77, s23, 0
	s_mov_b32 s78, -2
	s_mov_b64 s[22:23], 0
	ds_read_b128 v[156:159], v149
	ds_read_b128 v[160:163], v149 offset:1024
	ds_read_b128 v[164:167], v149 offset:2048
	ds_read_b128 v[168:171], v149 offset:3072
	ds_read_b128 v[172:175], v149 offset:16384
	ds_read_b128 v[176:179], v149 offset:17408
	ds_read_b128 v[180:183], v149 offset:18432
	ds_read_b128 v[184:187], v149 offset:19456
	s_add_u32 s24, s20, s22
	s_addc_u32 s25, s21, s23
	s_add_u32 s26, s24, 0x100
	s_addc_u32 s27, s25, 0
	s_add_u32 s24, s76, s22
	s_addc_u32 s25, s77, s23
	s_cmpk_eq_i32 s22, 0xf00
	s_cselect_b32 s25, s2, s25
	s_cselect_b32 s24, s3, s24
	s_cselect_b32 s27, s74, s27
	s_cselect_b32 s26, s75, s26
	v_lshl_add_u64 v[220:221], v[146:147], 0, s[22:23]
	v_lshl_add_u64 v[222:223], v[220:221], 0, s[6:7]
	s_add_i32 m0, s33, 0x8000
	ds_read_b128 v[188:191], v148
	ds_read_b128 v[192:195], v148 offset:1024
	ds_read_b128 v[196:199], v148 offset:2048
	ds_read_b128 v[200:203], v148 offset:3072
	ds_read_b128 v[204:207], v148 offset:4096
	ds_read_b128 v[208:211], v148 offset:5120
	ds_read_b128 v[212:215], v148 offset:6144
	ds_read_b128 v[216:219], v148 offset:7168
	global_load_lds_dwordx4 v[222:223], off
	v_lshl_add_u64 v[222:223], v[144:145], 0, s[22:23]
	v_lshl_add_u64 v[224:225], v[222:223], 0, s[6:7]
	s_add_i32 m0, s33, 0xa000
	v_lshl_add_u64 v[220:221], v[220:221], 0, s[8:9]
	global_load_lds_dwordx4 v[224:225], off
	s_add_i32 m0, s33, 0xc000
	s_nop 0
	global_load_lds_dwordx4 v[220:221], off
	v_lshl_add_u64 v[220:221], v[222:223], 0, s[8:9]
	s_add_i32 m0, s33, 0xe000
	s_nop 0
	global_load_lds_dwordx4 v[220:221], off
	s_waitcnt vmcnt(8)
	s_waitcnt lgkmcnt(0)
	s_barrier
	s_setprio 1
	s_waitcnt lgkmcnt(0)
	v_mfma_f32_16x16x32_bf16 v[126:129], v[156:159], v[188:191], 0
	v_mfma_f32_16x16x32_bf16 v[122:125], v[164:167], v[188:191], 0
	v_mfma_f32_16x16x32_bf16 v[114:117], v[156:159], v[196:199], 0
	v_mfma_f32_16x16x32_bf16 v[106:109], v[164:167], v[196:199], 0
	v_mfma_f32_16x16x32_bf16 v[94:97], v[156:159], v[204:207], 0
	v_mfma_f32_16x16x32_bf16 v[90:93], v[164:167], v[204:207], 0
	v_mfma_f32_16x16x32_bf16 v[82:85], v[156:159], v[212:215], 0
	v_mfma_f32_16x16x32_bf16 v[74:77], v[164:167], v[212:215], 0
	v_mfma_f32_16x16x32_bf16 v[126:129], v[160:163], v[192:195], v[126:129]
	v_mfma_f32_16x16x32_bf16 v[122:125], v[168:171], v[192:195], v[122:125]
	v_mfma_f32_16x16x32_bf16 v[114:117], v[160:163], v[200:203], v[114:117]
	v_mfma_f32_16x16x32_bf16 v[106:109], v[168:171], v[200:203], v[106:109]
	v_mfma_f32_16x16x32_bf16 v[94:97], v[160:163], v[208:211], v[94:97]
	v_mfma_f32_16x16x32_bf16 v[90:93], v[168:171], v[208:211], v[90:93]
	v_mfma_f32_16x16x32_bf16 v[82:85], v[160:163], v[216:219], v[82:85]
	v_mfma_f32_16x16x32_bf16 v[74:77], v[168:171], v[216:219], v[74:77]
	s_setprio 0
	s_setprio 1
	v_mfma_f32_16x16x32_bf16 v[118:121], v[172:175], v[188:191], 0
	v_mfma_f32_16x16x32_bf16 v[110:113], v[180:183], v[188:191], 0
	v_mfma_f32_16x16x32_bf16 v[102:105], v[172:175], v[196:199], 0
	v_mfma_f32_16x16x32_bf16 v[98:101], v[180:183], v[196:199], 0
	v_mfma_f32_16x16x32_bf16 v[86:89], v[172:175], v[204:207], 0
	v_mfma_f32_16x16x32_bf16 v[78:81], v[180:183], v[204:207], 0
	v_mfma_f32_16x16x32_bf16 v[70:73], v[172:175], v[212:215], 0
	v_mfma_f32_16x16x32_bf16 v[66:69], v[180:183], v[212:215], 0
	v_mfma_f32_16x16x32_bf16 v[118:121], v[176:179], v[192:195], v[118:121]
	v_mfma_f32_16x16x32_bf16 v[110:113], v[184:187], v[192:195], v[110:113]
	v_mfma_f32_16x16x32_bf16 v[102:105], v[176:179], v[200:203], v[102:105]
	v_mfma_f32_16x16x32_bf16 v[98:101], v[184:187], v[200:203], v[98:101]
	v_mfma_f32_16x16x32_bf16 v[86:89], v[176:179], v[208:211], v[86:89]
	v_mfma_f32_16x16x32_bf16 v[78:81], v[184:187], v[208:211], v[78:81]
	v_mfma_f32_16x16x32_bf16 v[70:73], v[176:179], v[216:219], v[70:73]
	v_mfma_f32_16x16x32_bf16 v[66:69], v[184:187], v[216:219], v[66:69]
	s_setprio 0
	s_barrier
	s_mov_b32 m0, s34
	v_lshl_add_u64 v[220:221], s[24:25], 0, v[134:135]
	s_add_u32 s80, s24, 0x80000
	ds_read_b128 v[188:191], v148 offset:16384
	ds_read_b128 v[192:195], v148 offset:17408
	ds_read_b128 v[196:199], v148 offset:18432
	ds_read_b128 v[200:203], v148 offset:19456
	ds_read_b128 v[204:207], v148 offset:20480
	ds_read_b128 v[208:211], v148 offset:21504
	ds_read_b128 v[212:215], v148 offset:22528
	ds_read_b128 v[216:219], v148 offset:23552
	global_load_lds_dwordx4 v[220:221], off
	v_lshl_add_u64 v[222:223], s[24:25], 0, v[130:131]
	s_mov_b32 m0, s35
	s_addc_u32 s81, s25, 0
	global_load_lds_dwordx4 v[222:223], off
	v_lshl_add_u64 v[224:225], s[80:81], 0, v[134:135]
	s_mov_b32 m0, s42
	s_nop 0
	global_load_lds_dwordx4 v[224:225], off
	v_lshl_add_u64 v[224:225], s[80:81], 0, v[130:131]
	s_mov_b32 m0, s43
	s_nop 0
	global_load_lds_dwordx4 v[224:225], off
	s_waitcnt vmcnt(6)
	s_waitcnt lgkmcnt(0)
	s_barrier
	s_setprio 1
	s_waitcnt lgkmcnt(0)
	v_mfma_f32_16x16x32_bf16 v[62:65], v[156:159], v[188:191], 0
	v_mfma_f32_16x16x32_bf16 v[58:61], v[164:167], v[188:191], 0
	v_mfma_f32_16x16x32_bf16 v[50:53], v[156:159], v[196:199], 0
	v_mfma_f32_16x16x32_bf16 v[42:45], v[164:167], v[196:199], 0
	v_mfma_f32_16x16x32_bf16 v[30:33], v[156:159], v[204:207], 0
	v_mfma_f32_16x16x32_bf16 v[26:29], v[164:167], v[204:207], 0
	v_mfma_f32_16x16x32_bf16 v[18:21], v[156:159], v[212:215], 0
	v_mfma_f32_16x16x32_bf16 v[10:13], v[164:167], v[212:215], 0
	v_mfma_f32_16x16x32_bf16 v[62:65], v[160:163], v[192:195], v[62:65]
	v_mfma_f32_16x16x32_bf16 v[58:61], v[168:171], v[192:195], v[58:61]
	v_mfma_f32_16x16x32_bf16 v[50:53], v[160:163], v[200:203], v[50:53]
	v_mfma_f32_16x16x32_bf16 v[42:45], v[168:171], v[200:203], v[42:45]
	v_mfma_f32_16x16x32_bf16 v[30:33], v[160:163], v[208:211], v[30:33]
	v_mfma_f32_16x16x32_bf16 v[26:29], v[168:171], v[208:211], v[26:29]
	v_mfma_f32_16x16x32_bf16 v[18:21], v[160:163], v[216:219], v[18:21]
	v_mfma_f32_16x16x32_bf16 v[10:13], v[168:171], v[216:219], v[10:13]
	s_setprio 0
	s_setprio 1
	v_mfma_f32_16x16x32_bf16 v[54:57], v[172:175], v[188:191], 0
	v_mfma_f32_16x16x32_bf16 v[46:49], v[180:183], v[188:191], 0
	v_mfma_f32_16x16x32_bf16 v[38:41], v[172:175], v[196:199], 0
	v_mfma_f32_16x16x32_bf16 v[34:37], v[180:183], v[196:199], 0
	v_mfma_f32_16x16x32_bf16 v[22:25], v[172:175], v[204:207], 0
	v_mfma_f32_16x16x32_bf16 v[14:17], v[180:183], v[204:207], 0
	v_mfma_f32_16x16x32_bf16 v[6:9], v[172:175], v[212:215], 0
	v_mfma_f32_16x16x32_bf16 v[2:5], v[180:183], v[212:215], 0
	v_mfma_f32_16x16x32_bf16 v[54:57], v[176:179], v[192:195], v[54:57]
	v_mfma_f32_16x16x32_bf16 v[46:49], v[184:187], v[192:195], v[46:49]
	v_mfma_f32_16x16x32_bf16 v[38:41], v[176:179], v[200:203], v[38:41]
	v_mfma_f32_16x16x32_bf16 v[34:37], v[184:187], v[200:203], v[34:37]
	v_mfma_f32_16x16x32_bf16 v[22:25], v[176:179], v[208:211], v[22:25]
	v_mfma_f32_16x16x32_bf16 v[14:17], v[184:187], v[208:211], v[14:17]
	v_mfma_f32_16x16x32_bf16 v[6:9], v[176:179], v[216:219], v[6:9]
	v_mfma_f32_16x16x32_bf16 v[2:5], v[184:187], v[216:219], v[2:5]
	s_setprio 0
	s_barrier
	s_branch .Lpeel_mid_p2

.Lpeel_mid_p2:
	ds_read_b128 v[156:159], v149 offset:32768
	ds_read_b128 v[160:163], v149 offset:33792
	ds_read_b128 v[164:167], v149 offset:34816
	ds_read_b128 v[168:171], v149 offset:35840
	ds_read_b128 v[172:175], v149 offset:49152
	ds_read_b128 v[176:179], v149 offset:50176
	ds_read_b128 v[180:183], v149 offset:51200
	ds_read_b128 v[184:187], v149 offset:52224
	s_mov_b32 m0, s33
	v_lshl_add_u64 v[224:225], s[26:27], 0, v[136:137]
	ds_read_b128 v[188:191], v148 offset:32768
	ds_read_b128 v[192:195], v148 offset:33792
	ds_read_b128 v[196:199], v148 offset:34816
	ds_read_b128 v[200:203], v148 offset:35840
	ds_read_b128 v[204:207], v148 offset:36864
	ds_read_b128 v[208:211], v148 offset:37888
	ds_read_b128 v[212:215], v148 offset:38912
	ds_read_b128 v[216:219], v148 offset:39936
	global_load_lds_dwordx4 v[224:225], off
	v_lshl_add_u64 v[224:225], s[26:27], 0, v[132:133]
	s_add_u32 s26, s26, 0x80000
	s_mov_b32 m0, s44
	s_addc_u32 s27, s27, 0
	global_load_lds_dwordx4 v[224:225], off
	v_lshl_add_u64 v[224:225], s[26:27], 0, v[136:137]
	s_mov_b32 m0, s45
	s_nop 0
	global_load_lds_dwordx4 v[224:225], off
	v_lshl_add_u64 v[224:225], s[26:27], 0, v[132:133]
	s_mov_b32 m0, s58
	s_nop 0
	global_load_lds_dwordx4 v[224:225], off
	s_waitcnt vmcnt(8)
	s_waitcnt lgkmcnt(0)
	s_barrier
	s_setprio 1
	s_waitcnt lgkmcnt(0)
	v_mfma_f32_16x16x32_bf16 v[126:129], v[156:159], v[188:191], v[126:129]
	v_mfma_f32_16x16x32_bf16 v[122:125], v[164:167], v[188:191], v[122:125]
	v_mfma_f32_16x16x32_bf16 v[114:117], v[156:159], v[196:199], v[114:117]
	v_mfma_f32_16x16x32_bf16 v[106:109], v[164:167], v[196:199], v[106:109]
	v_mfma_f32_16x16x32_bf16 v[94:97], v[156:159], v[204:207], v[94:97]
	v_mfma_f32_16x16x32_bf16 v[90:93], v[164:167], v[204:207], v[90:93]
	v_mfma_f32_16x16x32_bf16 v[82:85], v[156:159], v[212:215], v[82:85]
	v_mfma_f32_16x16x32_bf16 v[74:77], v[164:167], v[212:215], v[74:77]
	v_mfma_f32_16x16x32_bf16 v[126:129], v[160:163], v[192:195], v[126:129]
	v_mfma_f32_16x16x32_bf16 v[122:125], v[168:171], v[192:195], v[122:125]
	v_mfma_f32_16x16x32_bf16 v[114:117], v[160:163], v[200:203], v[114:117]
	v_mfma_f32_16x16x32_bf16 v[106:109], v[168:171], v[200:203], v[106:109]
	v_mfma_f32_16x16x32_bf16 v[94:97], v[160:163], v[208:211], v[94:97]
	v_mfma_f32_16x16x32_bf16 v[90:93], v[168:171], v[208:211], v[90:93]
	v_mfma_f32_16x16x32_bf16 v[82:85], v[160:163], v[216:219], v[82:85]
	v_mfma_f32_16x16x32_bf16 v[74:77], v[168:171], v[216:219], v[74:77]
	s_setprio 0
	s_setprio 1
	v_mfma_f32_16x16x32_bf16 v[118:121], v[172:175], v[188:191], v[118:121]
	v_mfma_f32_16x16x32_bf16 v[110:113], v[180:183], v[188:191], v[110:113]
	v_mfma_f32_16x16x32_bf16 v[102:105], v[172:175], v[196:199], v[102:105]
	v_mfma_f32_16x16x32_bf16 v[98:101], v[180:183], v[196:199], v[98:101]
	v_mfma_f32_16x16x32_bf16 v[86:89], v[172:175], v[204:207], v[86:89]
	v_mfma_f32_16x16x32_bf16 v[78:81], v[180:183], v[204:207], v[78:81]
	v_mfma_f32_16x16x32_bf16 v[70:73], v[172:175], v[212:215], v[70:73]
	v_mfma_f32_16x16x32_bf16 v[66:69], v[180:183], v[212:215], v[66:69]
	v_mfma_f32_16x16x32_bf16 v[118:121], v[176:179], v[192:195], v[118:121]
	v_mfma_f32_16x16x32_bf16 v[110:113], v[184:187], v[192:195], v[110:113]
	v_mfma_f32_16x16x32_bf16 v[102:105], v[176:179], v[200:203], v[102:105]
	v_mfma_f32_16x16x32_bf16 v[98:101], v[184:187], v[200:203], v[98:101]
	v_mfma_f32_16x16x32_bf16 v[86:89], v[176:179], v[208:211], v[86:89]
	v_mfma_f32_16x16x32_bf16 v[78:81], v[184:187], v[208:211], v[78:81]
	v_mfma_f32_16x16x32_bf16 v[70:73], v[176:179], v[216:219], v[70:73]
	v_mfma_f32_16x16x32_bf16 v[66:69], v[184:187], v[216:219], v[66:69]
	s_setprio 0
	s_barrier
	s_mov_b32 m0, s62
	v_lshl_add_u64 v[220:221], v[220:221], 0, s[6:7]
	s_add_u32 s24, s24, 0x80080
	ds_read_b128 v[188:191], v148 offset:49152
	ds_read_b128 v[192:195], v148 offset:50176
	ds_read_b128 v[196:199], v148 offset:51200
	ds_read_b128 v[200:203], v148 offset:52224
	ds_read_b128 v[204:207], v148 offset:53248
	ds_read_b128 v[208:211], v148 offset:54272
	ds_read_b128 v[212:215], v148 offset:55296
	ds_read_b128 v[216:219], v148 offset:56320
	global_load_lds_dwordx4 v[220:221], off
	v_lshl_add_u64 v[220:221], v[222:223], 0, s[6:7]
	s_mov_b32 m0, s63
	s_addc_u32 s25, s25, 0
	global_load_lds_dwordx4 v[220:221], off
	v_lshl_add_u64 v[220:221], s[24:25], 0, v[134:135]
	s_mov_b32 m0, s68
	s_nop 0
	global_load_lds_dwordx4 v[220:221], off
	v_lshl_add_u64 v[220:221], s[24:25], 0, v[130:131]
	s_mov_b32 m0, s69
	s_nop 0
	global_load_lds_dwordx4 v[220:221], off
	s_waitcnt vmcnt(6)
	s_waitcnt lgkmcnt(0)
	s_barrier
	s_setprio 1
	s_waitcnt lgkmcnt(0)
	v_mfma_f32_16x16x32_bf16 v[62:65], v[156:159], v[188:191], v[62:65]
	v_mfma_f32_16x16x32_bf16 v[58:61], v[164:167], v[188:191], v[58:61]
	v_mfma_f32_16x16x32_bf16 v[50:53], v[156:159], v[196:199], v[50:53]
	v_mfma_f32_16x16x32_bf16 v[42:45], v[164:167], v[196:199], v[42:45]
	v_mfma_f32_16x16x32_bf16 v[30:33], v[156:159], v[204:207], v[30:33]
	v_mfma_f32_16x16x32_bf16 v[26:29], v[164:167], v[204:207], v[26:29]
	v_mfma_f32_16x16x32_bf16 v[18:21], v[156:159], v[212:215], v[18:21]
	v_mfma_f32_16x16x32_bf16 v[10:13], v[164:167], v[212:215], v[10:13]
	v_mfma_f32_16x16x32_bf16 v[62:65], v[160:163], v[192:195], v[62:65]
	v_mfma_f32_16x16x32_bf16 v[58:61], v[168:171], v[192:195], v[58:61]
	v_mfma_f32_16x16x32_bf16 v[50:53], v[160:163], v[200:203], v[50:53]
	v_mfma_f32_16x16x32_bf16 v[42:45], v[168:171], v[200:203], v[42:45]
	v_mfma_f32_16x16x32_bf16 v[30:33], v[160:163], v[208:211], v[30:33]
	v_mfma_f32_16x16x32_bf16 v[26:29], v[168:171], v[208:211], v[26:29]
	v_mfma_f32_16x16x32_bf16 v[18:21], v[160:163], v[216:219], v[18:21]
	v_mfma_f32_16x16x32_bf16 v[10:13], v[168:171], v[216:219], v[10:13]
	s_setprio 0
	s_setprio 1
	v_mfma_f32_16x16x32_bf16 v[54:57], v[172:175], v[188:191], v[54:57]
	v_mfma_f32_16x16x32_bf16 v[46:49], v[180:183], v[188:191], v[46:49]
	v_mfma_f32_16x16x32_bf16 v[38:41], v[172:175], v[196:199], v[38:41]
	v_mfma_f32_16x16x32_bf16 v[34:37], v[180:183], v[196:199], v[34:37]
	v_mfma_f32_16x16x32_bf16 v[22:25], v[172:175], v[204:207], v[22:25]
	v_mfma_f32_16x16x32_bf16 v[14:17], v[180:183], v[204:207], v[14:17]
	v_mfma_f32_16x16x32_bf16 v[6:9], v[172:175], v[212:215], v[6:9]
	v_mfma_f32_16x16x32_bf16 v[2:5], v[180:183], v[212:215], v[2:5]
	v_mfma_f32_16x16x32_bf16 v[54:57], v[176:179], v[192:195], v[54:57]
	v_mfma_f32_16x16x32_bf16 v[46:49], v[184:187], v[192:195], v[46:49]
	v_mfma_f32_16x16x32_bf16 v[38:41], v[176:179], v[200:203], v[38:41]
	v_mfma_f32_16x16x32_bf16 v[34:37], v[184:187], v[200:203], v[34:37]
	v_mfma_f32_16x16x32_bf16 v[22:25], v[176:179], v[208:211], v[22:25]
	v_mfma_f32_16x16x32_bf16 v[14:17], v[184:187], v[208:211], v[14:17]
	v_mfma_f32_16x16x32_bf16 v[6:9], v[176:179], v[216:219], v[6:9]
	v_mfma_f32_16x16x32_bf16 v[2:5], v[184:187], v[216:219], v[2:5]
	s_setprio 0
	s_barrier
	s_add_i32 s78, s78, 2
	s_add_u32 s22, s22, 0x100
	s_addc_u32 s23, s23, 0
	s_cmp_gt_u32 s78, 29
	s_cbranch_scc0 .LBB0_326
	s_and_b64 vcc, exec, s[10:11]
	s_cbranch_vccz .LBB0_329
	s_barrier

.LBB0_720:
	s_ashr_i32 s15, s12, 31
	s_mov_b32 s14, s12
	s_lshl_b64 s[14:15], s[14:15], 20
	s_add_u32 s14, s28, s14
	s_addc_u32 s15, s29, s15
	s_and_b64 s[16:17], s[2:3], exec
	s_cselect_b32 s59, s15, s21
	s_cselect_b32 s60, s14, s20
	s_ashr_i32 s17, s13, 31
	s_mov_b32 s16, s13
	s_lshl_b64 s[16:17], s[16:17], 20
	s_add_u32 s16, s30, s16
	s_addc_u32 s17, s31, s17
	s_and_b64 s[2:3], s[2:3], exec
	s_cselect_b32 s2, s17, s23
	s_cselect_b32 s3, s16, s22
	s_add_u32 s61, s22, 0x100
	v_lshl_add_u64 v[144:145], s[20:21], 0, v[140:141]
	v_lshl_add_u64 v[146:147], s[20:21], 0, v[142:143]
	s_addc_u32 s62, s23, 0
	s_mov_b32 s63, -2
	s_mov_b64 s[22:23], 0
	ds_read_b128 v[156:159], v149
	ds_read_b128 v[160:163], v149 offset:1024
	ds_read_b128 v[164:167], v149 offset:2048
	ds_read_b128 v[168:171], v149 offset:3072
	ds_read_b128 v[172:175], v149 offset:16384
	ds_read_b128 v[176:179], v149 offset:17408
	ds_read_b128 v[180:183], v149 offset:18432
	ds_read_b128 v[184:187], v149 offset:19456
	s_add_u32 s24, s20, s22
	s_addc_u32 s25, s21, s23
	s_add_u32 s26, s24, 0x100
	s_addc_u32 s27, s25, 0
	s_add_u32 s24, s61, s22
	s_addc_u32 s25, s62, s23
	s_cmpk_eq_i32 s22, 0xf00
	s_cselect_b32 s25, s2, s25
	s_cselect_b32 s24, s3, s24
	s_cselect_b32 s27, s59, s27
	s_cselect_b32 s26, s60, s26
	v_lshl_add_u64 v[220:221], v[146:147], 0, s[22:23]
	v_lshl_add_u64 v[222:223], v[220:221], 0, s[6:7]
	s_add_i32 m0, s33, 0x8000
	ds_read_b128 v[188:191], v148
	ds_read_b128 v[192:195], v148 offset:1024
	ds_read_b128 v[196:199], v148 offset:2048
	ds_read_b128 v[200:203], v148 offset:3072
	ds_read_b128 v[204:207], v148 offset:4096
	ds_read_b128 v[208:211], v148 offset:5120
	ds_read_b128 v[212:215], v148 offset:6144
	ds_read_b128 v[216:219], v148 offset:7168
	global_load_lds_dwordx4 v[222:223], off
	v_lshl_add_u64 v[222:223], v[144:145], 0, s[22:23]
	v_lshl_add_u64 v[224:225], v[222:223], 0, s[6:7]
	s_add_i32 m0, s33, 0xa000
	v_lshl_add_u64 v[220:221], v[220:221], 0, s[8:9]
	global_load_lds_dwordx4 v[224:225], off
	s_add_i32 m0, s33, 0xc000
	s_nop 0
	global_load_lds_dwordx4 v[220:221], off
	v_lshl_add_u64 v[220:221], v[222:223], 0, s[8:9]
	s_add_i32 m0, s33, 0xe000
	s_nop 0
	global_load_lds_dwordx4 v[220:221], off
	s_waitcnt vmcnt(8)
	s_waitcnt lgkmcnt(0)
	s_barrier
	s_setprio 1
	s_waitcnt lgkmcnt(0)
	v_mfma_f32_16x16x32_bf16 v[126:129], v[156:159], v[188:191], 0
	v_mfma_f32_16x16x32_bf16 v[122:125], v[164:167], v[188:191], 0
	v_mfma_f32_16x16x32_bf16 v[114:117], v[156:159], v[196:199], 0
	v_mfma_f32_16x16x32_bf16 v[106:109], v[164:167], v[196:199], 0
	v_mfma_f32_16x16x32_bf16 v[94:97], v[156:159], v[204:207], 0
	v_mfma_f32_16x16x32_bf16 v[90:93], v[164:167], v[204:207], 0
	v_mfma_f32_16x16x32_bf16 v[82:85], v[156:159], v[212:215], 0
	v_mfma_f32_16x16x32_bf16 v[74:77], v[164:167], v[212:215], 0
	v_mfma_f32_16x16x32_bf16 v[126:129], v[160:163], v[192:195], v[126:129]
	v_mfma_f32_16x16x32_bf16 v[122:125], v[168:171], v[192:195], v[122:125]
	v_mfma_f32_16x16x32_bf16 v[114:117], v[160:163], v[200:203], v[114:117]
	v_mfma_f32_16x16x32_bf16 v[106:109], v[168:171], v[200:203], v[106:109]
	v_mfma_f32_16x16x32_bf16 v[94:97], v[160:163], v[208:211], v[94:97]
	v_mfma_f32_16x16x32_bf16 v[90:93], v[168:171], v[208:211], v[90:93]
	v_mfma_f32_16x16x32_bf16 v[82:85], v[160:163], v[216:219], v[82:85]
	v_mfma_f32_16x16x32_bf16 v[74:77], v[168:171], v[216:219], v[74:77]
	s_setprio 0
	s_setprio 1
	v_mfma_f32_16x16x32_bf16 v[118:121], v[172:175], v[188:191], 0
	v_mfma_f32_16x16x32_bf16 v[110:113], v[180:183], v[188:191], 0
	v_mfma_f32_16x16x32_bf16 v[102:105], v[172:175], v[196:199], 0
	v_mfma_f32_16x16x32_bf16 v[98:101], v[180:183], v[196:199], 0
	v_mfma_f32_16x16x32_bf16 v[86:89], v[172:175], v[204:207], 0
	v_mfma_f32_16x16x32_bf16 v[78:81], v[180:183], v[204:207], 0
	v_mfma_f32_16x16x32_bf16 v[70:73], v[172:175], v[212:215], 0
	v_mfma_f32_16x16x32_bf16 v[66:69], v[180:183], v[212:215], 0
	v_mfma_f32_16x16x32_bf16 v[118:121], v[176:179], v[192:195], v[118:121]
	v_mfma_f32_16x16x32_bf16 v[110:113], v[184:187], v[192:195], v[110:113]
	v_mfma_f32_16x16x32_bf16 v[102:105], v[176:179], v[200:203], v[102:105]
	v_mfma_f32_16x16x32_bf16 v[98:101], v[184:187], v[200:203], v[98:101]
	v_mfma_f32_16x16x32_bf16 v[86:89], v[176:179], v[208:211], v[86:89]
	v_mfma_f32_16x16x32_bf16 v[78:81], v[184:187], v[208:211], v[78:81]
	v_mfma_f32_16x16x32_bf16 v[70:73], v[176:179], v[216:219], v[70:73]
	v_mfma_f32_16x16x32_bf16 v[66:69], v[184:187], v[216:219], v[66:69]
	s_setprio 0
	s_barrier
	s_mov_b32 m0, s34
	v_lshl_add_u64 v[220:221], s[24:25], 0, v[134:135]
	s_add_u32 s64, s24, 0x80000
	ds_read_b128 v[188:191], v148 offset:16384
	ds_read_b128 v[192:195], v148 offset:17408
	ds_read_b128 v[196:199], v148 offset:18432
	ds_read_b128 v[200:203], v148 offset:19456
	ds_read_b128 v[204:207], v148 offset:20480
	ds_read_b128 v[208:211], v148 offset:21504
	ds_read_b128 v[212:215], v148 offset:22528
	ds_read_b128 v[216:219], v148 offset:23552
	global_load_lds_dwordx4 v[220:221], off
	v_lshl_add_u64 v[222:223], s[24:25], 0, v[130:131]
	s_mov_b32 m0, s35
	s_addc_u32 s65, s25, 0
	global_load_lds_dwordx4 v[222:223], off
	v_lshl_add_u64 v[224:225], s[64:65], 0, v[134:135]
	s_mov_b32 m0, s36
	s_nop 0
	global_load_lds_dwordx4 v[224:225], off
	v_lshl_add_u64 v[224:225], s[64:65], 0, v[130:131]
	s_mov_b32 m0, s37
	s_nop 0
	global_load_lds_dwordx4 v[224:225], off
	s_waitcnt vmcnt(6)
	s_waitcnt lgkmcnt(0)
	s_barrier
	s_setprio 1
	s_waitcnt lgkmcnt(0)
	v_mfma_f32_16x16x32_bf16 v[62:65], v[156:159], v[188:191], 0
	v_mfma_f32_16x16x32_bf16 v[58:61], v[164:167], v[188:191], 0
	v_mfma_f32_16x16x32_bf16 v[50:53], v[156:159], v[196:199], 0
	v_mfma_f32_16x16x32_bf16 v[42:45], v[164:167], v[196:199], 0
	v_mfma_f32_16x16x32_bf16 v[30:33], v[156:159], v[204:207], 0
	v_mfma_f32_16x16x32_bf16 v[26:29], v[164:167], v[204:207], 0
	v_mfma_f32_16x16x32_bf16 v[18:21], v[156:159], v[212:215], 0
	v_mfma_f32_16x16x32_bf16 v[10:13], v[164:167], v[212:215], 0
	v_mfma_f32_16x16x32_bf16 v[62:65], v[160:163], v[192:195], v[62:65]
	v_mfma_f32_16x16x32_bf16 v[58:61], v[168:171], v[192:195], v[58:61]
	v_mfma_f32_16x16x32_bf16 v[50:53], v[160:163], v[200:203], v[50:53]
	v_mfma_f32_16x16x32_bf16 v[42:45], v[168:171], v[200:203], v[42:45]
	v_mfma_f32_16x16x32_bf16 v[30:33], v[160:163], v[208:211], v[30:33]
	v_mfma_f32_16x16x32_bf16 v[26:29], v[168:171], v[208:211], v[26:29]
	v_mfma_f32_16x16x32_bf16 v[18:21], v[160:163], v[216:219], v[18:21]
	v_mfma_f32_16x16x32_bf16 v[10:13], v[168:171], v[216:219], v[10:13]
	s_setprio 0
	s_setprio 1
	v_mfma_f32_16x16x32_bf16 v[54:57], v[172:175], v[188:191], 0
	v_mfma_f32_16x16x32_bf16 v[46:49], v[180:183], v[188:191], 0
	v_mfma_f32_16x16x32_bf16 v[38:41], v[172:175], v[196:199], 0
	v_mfma_f32_16x16x32_bf16 v[34:37], v[180:183], v[196:199], 0
	v_mfma_f32_16x16x32_bf16 v[22:25], v[172:175], v[204:207], 0
	v_mfma_f32_16x16x32_bf16 v[14:17], v[180:183], v[204:207], 0
	v_mfma_f32_16x16x32_bf16 v[6:9], v[172:175], v[212:215], 0
	v_mfma_f32_16x16x32_bf16 v[2:5], v[180:183], v[212:215], 0
	v_mfma_f32_16x16x32_bf16 v[54:57], v[176:179], v[192:195], v[54:57]
	v_mfma_f32_16x16x32_bf16 v[46:49], v[184:187], v[192:195], v[46:49]
	v_mfma_f32_16x16x32_bf16 v[38:41], v[176:179], v[200:203], v[38:41]
	v_mfma_f32_16x16x32_bf16 v[34:37], v[184:187], v[200:203], v[34:37]
	v_mfma_f32_16x16x32_bf16 v[22:25], v[176:179], v[208:211], v[22:25]
	v_mfma_f32_16x16x32_bf16 v[14:17], v[184:187], v[208:211], v[14:17]
	v_mfma_f32_16x16x32_bf16 v[6:9], v[176:179], v[216:219], v[6:9]
	v_mfma_f32_16x16x32_bf16 v[2:5], v[184:187], v[216:219], v[2:5]
	s_setprio 0
	s_barrier
	s_branch .Lpeel_mid_p6

.Lpeel_mid_p6:
	ds_read_b128 v[156:159], v149 offset:32768
	ds_read_b128 v[160:163], v149 offset:33792
	ds_read_b128 v[164:167], v149 offset:34816
	ds_read_b128 v[168:171], v149 offset:35840
	ds_read_b128 v[172:175], v149 offset:49152
	ds_read_b128 v[176:179], v149 offset:50176
	ds_read_b128 v[180:183], v149 offset:51200
	ds_read_b128 v[184:187], v149 offset:52224
	s_mov_b32 m0, s33
	v_lshl_add_u64 v[224:225], s[26:27], 0, v[136:137]
	ds_read_b128 v[188:191], v148 offset:32768
	ds_read_b128 v[192:195], v148 offset:33792
	ds_read_b128 v[196:199], v148 offset:34816
	ds_read_b128 v[200:203], v148 offset:35840
	ds_read_b128 v[204:207], v148 offset:36864
	ds_read_b128 v[208:211], v148 offset:37888
	ds_read_b128 v[212:215], v148 offset:38912
	ds_read_b128 v[216:219], v148 offset:39936
	global_load_lds_dwordx4 v[224:225], off
	v_lshl_add_u64 v[224:225], s[26:27], 0, v[132:133]
	s_add_u32 s26, s26, 0x80000
	s_mov_b32 m0, s38
	s_addc_u32 s27, s27, 0
	global_load_lds_dwordx4 v[224:225], off
	v_lshl_add_u64 v[224:225], s[26:27], 0, v[136:137]
	s_mov_b32 m0, s39
	s_nop 0
	global_load_lds_dwordx4 v[224:225], off
	v_lshl_add_u64 v[224:225], s[26:27], 0, v[132:133]
	s_mov_b32 m0, s40
	s_nop 0
	global_load_lds_dwordx4 v[224:225], off
	s_waitcnt vmcnt(8)
	s_waitcnt lgkmcnt(0)
	s_barrier
	s_setprio 1
	s_waitcnt lgkmcnt(0)
	v_mfma_f32_16x16x32_bf16 v[126:129], v[156:159], v[188:191], v[126:129]
	v_mfma_f32_16x16x32_bf16 v[122:125], v[164:167], v[188:191], v[122:125]
	v_mfma_f32_16x16x32_bf16 v[114:117], v[156:159], v[196:199], v[114:117]
	v_mfma_f32_16x16x32_bf16 v[106:109], v[164:167], v[196:199], v[106:109]
	v_mfma_f32_16x16x32_bf16 v[94:97], v[156:159], v[204:207], v[94:97]
	v_mfma_f32_16x16x32_bf16 v[90:93], v[164:167], v[204:207], v[90:93]
	v_mfma_f32_16x16x32_bf16 v[82:85], v[156:159], v[212:215], v[82:85]
	v_mfma_f32_16x16x32_bf16 v[74:77], v[164:167], v[212:215], v[74:77]
	v_mfma_f32_16x16x32_bf16 v[126:129], v[160:163], v[192:195], v[126:129]
	v_mfma_f32_16x16x32_bf16 v[122:125], v[168:171], v[192:195], v[122:125]
	v_mfma_f32_16x16x32_bf16 v[114:117], v[160:163], v[200:203], v[114:117]
	v_mfma_f32_16x16x32_bf16 v[106:109], v[168:171], v[200:203], v[106:109]
	v_mfma_f32_16x16x32_bf16 v[94:97], v[160:163], v[208:211], v[94:97]
	v_mfma_f32_16x16x32_bf16 v[90:93], v[168:171], v[208:211], v[90:93]
	v_mfma_f32_16x16x32_bf16 v[82:85], v[160:163], v[216:219], v[82:85]
	v_mfma_f32_16x16x32_bf16 v[74:77], v[168:171], v[216:219], v[74:77]
	s_setprio 0
	s_setprio 1
	v_mfma_f32_16x16x32_bf16 v[118:121], v[172:175], v[188:191], v[118:121]
	v_mfma_f32_16x16x32_bf16 v[110:113], v[180:183], v[188:191], v[110:113]
	v_mfma_f32_16x16x32_bf16 v[102:105], v[172:175], v[196:199], v[102:105]
	v_mfma_f32_16x16x32_bf16 v[98:101], v[180:183], v[196:199], v[98:101]
	v_mfma_f32_16x16x32_bf16 v[86:89], v[172:175], v[204:207], v[86:89]
	v_mfma_f32_16x16x32_bf16 v[78:81], v[180:183], v[204:207], v[78:81]
	v_mfma_f32_16x16x32_bf16 v[70:73], v[172:175], v[212:215], v[70:73]
	v_mfma_f32_16x16x32_bf16 v[66:69], v[180:183], v[212:215], v[66:69]
	v_mfma_f32_16x16x32_bf16 v[118:121], v[176:179], v[192:195], v[118:121]
	v_mfma_f32_16x16x32_bf16 v[110:113], v[184:187], v[192:195], v[110:113]
	v_mfma_f32_16x16x32_bf16 v[102:105], v[176:179], v[200:203], v[102:105]
	v_mfma_f32_16x16x32_bf16 v[98:101], v[184:187], v[200:203], v[98:101]
	v_mfma_f32_16x16x32_bf16 v[86:89], v[176:179], v[208:211], v[86:89]
	v_mfma_f32_16x16x32_bf16 v[78:81], v[184:187], v[208:211], v[78:81]
	v_mfma_f32_16x16x32_bf16 v[70:73], v[176:179], v[216:219], v[70:73]
	v_mfma_f32_16x16x32_bf16 v[66:69], v[184:187], v[216:219], v[66:69]
	s_setprio 0
	s_barrier
	s_mov_b32 m0, s42
	v_lshl_add_u64 v[220:221], v[220:221], 0, s[6:7]
	s_add_u32 s24, s24, 0x80080
	ds_read_b128 v[188:191], v148 offset:49152
	ds_read_b128 v[192:195], v148 offset:50176
	ds_read_b128 v[196:199], v148 offset:51200
	ds_read_b128 v[200:203], v148 offset:52224
	ds_read_b128 v[204:207], v148 offset:53248
	ds_read_b128 v[208:211], v148 offset:54272
	ds_read_b128 v[212:215], v148 offset:55296
	ds_read_b128 v[216:219], v148 offset:56320
	global_load_lds_dwordx4 v[220:221], off
	v_lshl_add_u64 v[220:221], v[222:223], 0, s[6:7]
	s_mov_b32 m0, s43
	s_addc_u32 s25, s25, 0
	global_load_lds_dwordx4 v[220:221], off
	v_lshl_add_u64 v[220:221], s[24:25], 0, v[134:135]
	s_mov_b32 m0, s44
	s_nop 0
	global_load_lds_dwordx4 v[220:221], off
	v_lshl_add_u64 v[220:221], s[24:25], 0, v[130:131]
	s_mov_b32 m0, s45
	s_nop 0
	global_load_lds_dwordx4 v[220:221], off
	s_waitcnt vmcnt(6)
	s_waitcnt lgkmcnt(0)
	s_barrier
	s_setprio 1
	s_waitcnt lgkmcnt(0)
	v_mfma_f32_16x16x32_bf16 v[62:65], v[156:159], v[188:191], v[62:65]
	v_mfma_f32_16x16x32_bf16 v[58:61], v[164:167], v[188:191], v[58:61]
	v_mfma_f32_16x16x32_bf16 v[50:53], v[156:159], v[196:199], v[50:53]
	v_mfma_f32_16x16x32_bf16 v[42:45], v[164:167], v[196:199], v[42:45]
	v_mfma_f32_16x16x32_bf16 v[30:33], v[156:159], v[204:207], v[30:33]
	v_mfma_f32_16x16x32_bf16 v[26:29], v[164:167], v[204:207], v[26:29]
	v_mfma_f32_16x16x32_bf16 v[18:21], v[156:159], v[212:215], v[18:21]
	v_mfma_f32_16x16x32_bf16 v[10:13], v[164:167], v[212:215], v[10:13]
	v_mfma_f32_16x16x32_bf16 v[62:65], v[160:163], v[192:195], v[62:65]
	v_mfma_f32_16x16x32_bf16 v[58:61], v[168:171], v[192:195], v[58:61]
	v_mfma_f32_16x16x32_bf16 v[50:53], v[160:163], v[200:203], v[50:53]
	v_mfma_f32_16x16x32_bf16 v[42:45], v[168:171], v[200:203], v[42:45]
	v_mfma_f32_16x16x32_bf16 v[30:33], v[160:163], v[208:211], v[30:33]
	v_mfma_f32_16x16x32_bf16 v[26:29], v[168:171], v[208:211], v[26:29]
	v_mfma_f32_16x16x32_bf16 v[18:21], v[160:163], v[216:219], v[18:21]
	v_mfma_f32_16x16x32_bf16 v[10:13], v[168:171], v[216:219], v[10:13]
	s_setprio 0
	s_setprio 1
	v_mfma_f32_16x16x32_bf16 v[54:57], v[172:175], v[188:191], v[54:57]
	v_mfma_f32_16x16x32_bf16 v[46:49], v[180:183], v[188:191], v[46:49]
	v_mfma_f32_16x16x32_bf16 v[38:41], v[172:175], v[196:199], v[38:41]
	v_mfma_f32_16x16x32_bf16 v[34:37], v[180:183], v[196:199], v[34:37]
	v_mfma_f32_16x16x32_bf16 v[22:25], v[172:175], v[204:207], v[22:25]
	v_mfma_f32_16x16x32_bf16 v[14:17], v[180:183], v[204:207], v[14:17]
	v_mfma_f32_16x16x32_bf16 v[6:9], v[172:175], v[212:215], v[6:9]
	v_mfma_f32_16x16x32_bf16 v[2:5], v[180:183], v[212:215], v[2:5]
	v_mfma_f32_16x16x32_bf16 v[54:57], v[176:179], v[192:195], v[54:57]
	v_mfma_f32_16x16x32_bf16 v[46:49], v[184:187], v[192:195], v[46:49]
	v_mfma_f32_16x16x32_bf16 v[38:41], v[176:179], v[200:203], v[38:41]
	v_mfma_f32_16x16x32_bf16 v[34:37], v[184:187], v[200:203], v[34:37]
	v_mfma_f32_16x16x32_bf16 v[22:25], v[176:179], v[208:211], v[22:25]
	v_mfma_f32_16x16x32_bf16 v[14:17], v[184:187], v[208:211], v[14:17]
	v_mfma_f32_16x16x32_bf16 v[6:9], v[176:179], v[216:219], v[6:9]
	v_mfma_f32_16x16x32_bf16 v[2:5], v[184:187], v[216:219], v[2:5]
	s_setprio 0
	s_barrier
	s_add_i32 s63, s63, 2
	s_add_u32 s22, s22, 0x100
	s_addc_u32 s23, s23, 0
	s_cmp_gt_u32 s63, 29
	s_cbranch_scc0 .LBB0_721
	s_and_b64 vcc, exec, s[10:11]
	s_cbranch_vccz .LBB0_724
	s_barrier

.LBB0_1146:
	s_ashr_i32 s17, s14, 31
	s_mov_b32 s16, s14
	s_lshl_b64 s[16:17], s[16:17], 19
	s_add_u32 s16, s13, s16
	s_addc_u32 s17, s30, s17
	s_and_b64 s[18:19], s[2:3], exec
	s_cselect_b32 s55, s17, s23
	s_cselect_b32 s56, s16, s22
	s_ashr_i32 s19, s15, 31
	s_mov_b32 s18, s15
	s_lshl_b64 s[18:19], s[18:19], 19
	s_add_u32 s18, s31, s18
	s_addc_u32 s19, s33, s19
	s_and_b64 s[2:3], s[2:3], exec
	s_cselect_b32 s2, s19, s25
	s_cselect_b32 s3, s18, s24
	s_add_u32 s57, s24, 0x100
	v_lshl_add_u64 v[176:177], s[22:23], 0, v[172:173]
	v_lshl_add_u64 v[178:179], s[22:23], 0, v[174:175]
	s_addc_u32 s58, s25, 0
	s_mov_b32 s59, -2
	s_mov_b64 s[24:25], 0
	ds_read_b128 v[18:21], v185
	ds_read_b128 v[22:25], v185 offset:1024
	ds_read_b128 v[26:29], v185 offset:2048
	ds_read_b128 v[30:33], v185 offset:3072
	ds_read_b128 v[2:5], v185 offset:16384
	ds_read_b128 v[6:9], v185 offset:17408
	ds_read_b128 v[10:13], v185 offset:18432
	ds_read_b128 v[14:17], v185 offset:19456
	s_add_u32 s26, s22, s24
	s_addc_u32 s27, s23, s25
	s_add_u32 s28, s26, 0x100
	s_addc_u32 s29, s27, 0
	s_add_u32 s26, s57, s24
	s_addc_u32 s27, s58, s25
	s_cmpk_eq_i32 s24, 0x700
	s_cselect_b32 s27, s2, s27
	s_cselect_b32 s26, s3, s26
	s_cselect_b32 s29, s55, s29
	s_cselect_b32 s28, s56, s28
	v_lshl_add_u64 v[180:181], v[178:179], 0, s[24:25]
	v_lshl_add_u64 v[182:183], v[180:181], 0, s[6:7]
	s_add_i32 m0, s34, 0x8000
	ds_read_b128 v[190:193], v184
	ds_read_b128 v[194:197], v184 offset:1024
	ds_read_b128 v[198:201], v184 offset:2048
	ds_read_b128 v[202:205], v184 offset:3072
	ds_read_b128 v[206:209], v184 offset:4096
	ds_read_b128 v[210:213], v184 offset:5120
	ds_read_b128 v[214:217], v184 offset:6144
	ds_read_b128 v[218:221], v184 offset:7168
	global_load_lds_dwordx4 v[182:183], off
	v_lshl_add_u64 v[182:183], v[176:177], 0, s[24:25]
	v_lshl_add_u64 v[222:223], v[182:183], 0, s[6:7]
	s_add_i32 m0, s34, 0xa000
	v_lshl_add_u64 v[180:181], v[180:181], 0, s[8:9]
	global_load_lds_dwordx4 v[222:223], off
	s_add_i32 m0, s34, 0xc000
	s_nop 0
	global_load_lds_dwordx4 v[180:181], off
	v_lshl_add_u64 v[180:181], v[182:183], 0, s[8:9]
	s_add_i32 m0, s34, 0xe000
	s_nop 0
	global_load_lds_dwordx4 v[180:181], off
	s_waitcnt vmcnt(8)
	s_waitcnt lgkmcnt(0)
	s_barrier
	s_setprio 1
	s_waitcnt lgkmcnt(0)
	v_mfma_f32_16x16x128_f8f6f4 v[158:161], v[18:25], v[190:197], 0
	v_mfma_f32_16x16x128_f8f6f4 v[154:157], v[26:33], v[190:197], 0
	v_mfma_f32_16x16x128_f8f6f4 v[150:153], v[18:25], v[198:205], 0
	v_mfma_f32_16x16x128_f8f6f4 v[146:149], v[26:33], v[198:205], 0
	v_mfma_f32_16x16x128_f8f6f4 v[142:145], v[18:25], v[206:213], 0
	v_mfma_f32_16x16x128_f8f6f4 v[134:137], v[26:33], v[206:213], 0
	v_mfma_f32_16x16x128_f8f6f4 v[110:113], v[18:25], v[214:221], 0
	v_mfma_f32_16x16x128_f8f6f4 v[106:109], v[26:33], v[214:221], 0
	s_setprio 0
	s_setprio 1
	v_mfma_f32_16x16x128_f8f6f4 v[138:141], v[2:9], v[190:197], 0
	v_mfma_f32_16x16x128_f8f6f4 v[130:133], v[10:17], v[190:197], 0
	v_mfma_f32_16x16x128_f8f6f4 v[126:129], v[2:9], v[198:205], 0
	v_mfma_f32_16x16x128_f8f6f4 v[122:125], v[10:17], v[198:205], 0
	v_mfma_f32_16x16x128_f8f6f4 v[118:121], v[2:9], v[206:213], 0
	v_mfma_f32_16x16x128_f8f6f4 v[114:117], v[10:17], v[206:213], 0
	v_mfma_f32_16x16x128_f8f6f4 v[102:105], v[2:9], v[214:221], 0
	v_mfma_f32_16x16x128_f8f6f4 v[98:101], v[10:17], v[214:221], 0
	s_setprio 0
	s_barrier
	s_mov_b32 m0, s35
	v_lshl_add_u64 v[180:181], s[26:27], 0, v[166:167]
	s_add_u32 s60, s26, 0x40000
	ds_read_b128 v[190:193], v184 offset:16384
	ds_read_b128 v[194:197], v184 offset:17408
	ds_read_b128 v[198:201], v184 offset:18432
	ds_read_b128 v[202:205], v184 offset:19456
	ds_read_b128 v[206:209], v184 offset:20480
	ds_read_b128 v[210:213], v184 offset:21504
	ds_read_b128 v[214:217], v184 offset:22528
	ds_read_b128 v[218:221], v184 offset:23552
	global_load_lds_dwordx4 v[180:181], off
	v_lshl_add_u64 v[182:183], s[26:27], 0, v[162:163]
	s_mov_b32 m0, s36
	s_addc_u32 s61, s27, 0
	global_load_lds_dwordx4 v[182:183], off
	v_lshl_add_u64 v[222:223], s[60:61], 0, v[166:167]
	s_mov_b32 m0, s37
	s_nop 0
	global_load_lds_dwordx4 v[222:223], off
	v_lshl_add_u64 v[222:223], s[60:61], 0, v[162:163]
	s_mov_b32 m0, s38
	s_nop 0
	global_load_lds_dwordx4 v[222:223], off
	s_waitcnt vmcnt(6)
	s_waitcnt lgkmcnt(0)
	s_barrier
	s_setprio 1
	s_waitcnt lgkmcnt(0)
	v_mfma_f32_16x16x128_f8f6f4 v[94:97], v[18:25], v[190:197], 0
	v_mfma_f32_16x16x128_f8f6f4 v[90:93], v[26:33], v[190:197], 0
	v_mfma_f32_16x16x128_f8f6f4 v[86:89], v[18:25], v[198:205], 0
	v_mfma_f32_16x16x128_f8f6f4 v[78:81], v[26:33], v[198:205], 0
	v_mfma_f32_16x16x128_f8f6f4 v[62:65], v[18:25], v[206:213], 0
	v_mfma_f32_16x16x128_f8f6f4 v[58:61], v[26:33], v[206:213], 0
	v_mfma_f32_16x16x128_f8f6f4 v[54:57], v[18:25], v[214:221], 0
	v_mfma_f32_16x16x128_f8f6f4 v[46:49], v[26:33], v[214:221], 0
	s_setprio 0
	s_setprio 1
	v_mfma_f32_16x16x128_f8f6f4 v[82:85], v[2:9], v[190:197], 0
	v_mfma_f32_16x16x128_f8f6f4 v[74:77], v[10:17], v[190:197], 0
	v_mfma_f32_16x16x128_f8f6f4 v[70:73], v[2:9], v[198:205], 0
	v_mfma_f32_16x16x128_f8f6f4 v[66:69], v[10:17], v[198:205], 0
	v_mfma_f32_16x16x128_f8f6f4 v[50:53], v[2:9], v[206:213], 0
	v_mfma_f32_16x16x128_f8f6f4 v[42:45], v[10:17], v[206:213], 0
	v_mfma_f32_16x16x128_f8f6f4 v[38:41], v[2:9], v[214:221], 0
	v_mfma_f32_16x16x128_f8f6f4 v[34:37], v[10:17], v[214:221], 0
	s_setprio 0
	s_barrier
	s_branch .Lpeel_mid_p10

.Lpeel_mid_p10:
	ds_read_b128 v[2:5], v185 offset:32768
	ds_read_b128 v[6:9], v185 offset:33792
	ds_read_b128 v[10:13], v185 offset:34816
	ds_read_b128 v[14:17], v185 offset:35840
	ds_read_b128 v[18:21], v185 offset:49152
	ds_read_b128 v[22:25], v185 offset:50176
	ds_read_b128 v[26:29], v185 offset:51200
	ds_read_b128 v[30:33], v185 offset:52224
	s_mov_b32 m0, s34
	v_lshl_add_u64 v[222:223], s[28:29], 0, v[168:169]
	ds_read_b128 v[190:193], v184 offset:32768
	ds_read_b128 v[194:197], v184 offset:33792
	ds_read_b128 v[198:201], v184 offset:34816
	ds_read_b128 v[202:205], v184 offset:35840
	ds_read_b128 v[206:209], v184 offset:36864
	ds_read_b128 v[210:213], v184 offset:37888
	ds_read_b128 v[214:217], v184 offset:38912
	ds_read_b128 v[218:221], v184 offset:39936
	global_load_lds_dwordx4 v[222:223], off
	v_lshl_add_u64 v[222:223], s[28:29], 0, v[164:165]
	s_add_u32 s28, s28, 0x40000
	s_mov_b32 m0, s39
	s_addc_u32 s29, s29, 0
	global_load_lds_dwordx4 v[222:223], off
	v_lshl_add_u64 v[222:223], s[28:29], 0, v[168:169]
	s_mov_b32 m0, s40
	s_nop 0
	global_load_lds_dwordx4 v[222:223], off
	v_lshl_add_u64 v[222:223], s[28:29], 0, v[164:165]
	s_mov_b32 m0, s41
	s_nop 0
	global_load_lds_dwordx4 v[222:223], off
	s_waitcnt vmcnt(8)
	s_waitcnt lgkmcnt(0)
	s_barrier
	s_setprio 1
	s_waitcnt lgkmcnt(0)
	v_mfma_f32_16x16x128_f8f6f4 v[158:161], v[2:9], v[190:197], v[158:161]
	v_mfma_f32_16x16x128_f8f6f4 v[154:157], v[10:17], v[190:197], v[154:157]
	v_mfma_f32_16x16x128_f8f6f4 v[150:153], v[2:9], v[198:205], v[150:153]
	v_mfma_f32_16x16x128_f8f6f4 v[146:149], v[10:17], v[198:205], v[146:149]
	v_mfma_f32_16x16x128_f8f6f4 v[142:145], v[2:9], v[206:213], v[142:145]
	v_mfma_f32_16x16x128_f8f6f4 v[134:137], v[10:17], v[206:213], v[134:137]
	v_mfma_f32_16x16x128_f8f6f4 v[110:113], v[2:9], v[214:221], v[110:113]
	v_mfma_f32_16x16x128_f8f6f4 v[106:109], v[10:17], v[214:221], v[106:109]
	s_setprio 0
	s_setprio 1
	v_mfma_f32_16x16x128_f8f6f4 v[138:141], v[18:25], v[190:197], v[138:141]
	v_mfma_f32_16x16x128_f8f6f4 v[130:133], v[26:33], v[190:197], v[130:133]
	v_mfma_f32_16x16x128_f8f6f4 v[126:129], v[18:25], v[198:205], v[126:129]
	v_mfma_f32_16x16x128_f8f6f4 v[122:125], v[26:33], v[198:205], v[122:125]
	v_mfma_f32_16x16x128_f8f6f4 v[118:121], v[18:25], v[206:213], v[118:121]
	v_mfma_f32_16x16x128_f8f6f4 v[114:117], v[26:33], v[206:213], v[114:117]
	v_mfma_f32_16x16x128_f8f6f4 v[102:105], v[18:25], v[214:221], v[102:105]
	v_mfma_f32_16x16x128_f8f6f4 v[98:101], v[26:33], v[214:221], v[98:101]
	s_setprio 0
	s_barrier
	s_mov_b32 m0, s43
	v_lshl_add_u64 v[180:181], v[180:181], 0, s[6:7]
	s_add_u32 s26, s26, 0x40080
	ds_read_b128 v[190:193], v184 offset:49152
	ds_read_b128 v[194:197], v184 offset:50176
	ds_read_b128 v[198:201], v184 offset:51200
	ds_read_b128 v[202:205], v184 offset:52224
	ds_read_b128 v[206:209], v184 offset:53248
	ds_read_b128 v[210:213], v184 offset:54272
	ds_read_b128 v[214:217], v184 offset:55296
	ds_read_b128 v[218:221], v184 offset:56320
	global_load_lds_dwordx4 v[180:181], off
	v_lshl_add_u64 v[180:181], v[182:183], 0, s[6:7]
	s_mov_b32 m0, s44
	s_addc_u32 s27, s27, 0
	global_load_lds_dwordx4 v[180:181], off
	v_lshl_add_u64 v[180:181], s[26:27], 0, v[166:167]
	s_mov_b32 m0, s45
	s_nop 0
	global_load_lds_dwordx4 v[180:181], off
	v_lshl_add_u64 v[180:181], s[26:27], 0, v[162:163]
	s_mov_b32 m0, s46
	s_nop 0
	global_load_lds_dwordx4 v[180:181], off
	s_waitcnt vmcnt(6)
	s_waitcnt lgkmcnt(0)
	s_barrier
	s_setprio 1
	s_waitcnt lgkmcnt(0)
	v_mfma_f32_16x16x128_f8f6f4 v[94:97], v[2:9], v[190:197], v[94:97]
	v_mfma_f32_16x16x128_f8f6f4 v[90:93], v[10:17], v[190:197], v[90:93]
	v_mfma_f32_16x16x128_f8f6f4 v[86:89], v[2:9], v[198:205], v[86:89]
	v_mfma_f32_16x16x128_f8f6f4 v[78:81], v[10:17], v[198:205], v[78:81]
	v_mfma_f32_16x16x128_f8f6f4 v[62:65], v[2:9], v[206:213], v[62:65]
	v_mfma_f32_16x16x128_f8f6f4 v[58:61], v[10:17], v[206:213], v[58:61]
	v_mfma_f32_16x16x128_f8f6f4 v[54:57], v[2:9], v[214:221], v[54:57]
	v_mfma_f32_16x16x128_f8f6f4 v[46:49], v[10:17], v[214:221], v[46:49]
	s_setprio 0
	s_setprio 1
	v_mfma_f32_16x16x128_f8f6f4 v[82:85], v[18:25], v[190:197], v[82:85]
	v_mfma_f32_16x16x128_f8f6f4 v[74:77], v[26:33], v[190:197], v[74:77]
	v_mfma_f32_16x16x128_f8f6f4 v[70:73], v[18:25], v[198:205], v[70:73]
	v_mfma_f32_16x16x128_f8f6f4 v[66:69], v[26:33], v[198:205], v[66:69]
	v_mfma_f32_16x16x128_f8f6f4 v[50:53], v[18:25], v[206:213], v[50:53]
	v_mfma_f32_16x16x128_f8f6f4 v[42:45], v[26:33], v[206:213], v[42:45]
	v_mfma_f32_16x16x128_f8f6f4 v[38:41], v[18:25], v[214:221], v[38:41]
	v_mfma_f32_16x16x128_f8f6f4 v[34:37], v[26:33], v[214:221], v[34:37]
	s_setprio 0
	s_barrier
	s_add_i32 s59, s59, 2
	s_add_u32 s24, s24, 0x100
	s_addc_u32 s25, s25, 0
	s_cmp_gt_u32 s59, 13
	s_cbranch_scc0 .LBB0_1147
	s_and_b64 vcc, exec, s[10:11]
	s_cbranch_vccz .LBB0_1150
	s_barrier
